# best + P1 row loop software-pipelined (next row's 8 KiB loads in flight during the current row's reduce/normalise/store)
# speedup vs baseline: 1.0335x; 1.0070x over previous
; #define in_x KARG(0)
; #define ctx KARG(2)
; __global__ void __launch_bounds__(NWAVES * 64, 2) mk_fwd(Args args) {
;     ...
;         for (int row = gw; row < MT; row += NGW) {
;             const float* src; const float* sh; const float* sc; int b;
;             if (row < M) { b = row / SEQ; src = in_x + (size_t)row * D; sh = MODX + b * MODW; sc = sh + D; }
;             else { b = NB; src = ctx + (size_t)(row - M) * D; sh = MODC; sc = MODC + D; }
;             f32x4 v[8]; float ss = 0.f;
; #pragma unroll
;             for (int j = 0; j < 8; ++j) v[j] = __builtin_nontemporal_load((const f32x4*)src + lane + 64 * j);
;             if (b != bcur) { bcur = b;
; #pragma unroll
;                 for (int j = 0; j < 8; ++j) { ps1[j] = ((const f32x4*)sc)[lane + 64 * j]; ps0[j] = ((const f32x4*)sh)[lane + 64 * j]; } }
.Lp1_entry:
	s_load_dwordx2 s[42:43], s[0:1], 0x0
	s_load_dwordx2 s[46:47], s[0:1], 0x10
	v_readlane_b32 s37, v255, 5
	v_lshlrev_b32_e32 v246, 4, v186
	v_add_u32_e32 v247, 0x1000, v246
	s_waitcnt lgkmcnt(0)
	s_cmpk_gt_i32 s24, 0x3fff
	s_cbranch_scc0 .Lp1_lat_a
	s_add_i32 s10, s24, 0xffffc000
	s_lshl_b64 s[18:19], s[10:11], 13
	s_add_u32 s20, s46, s18
	s_addc_u32 s21, s47, s19
	s_mov_b32 s10, 4
	s_mov_b64 s[18:19], s[4:5]
	s_mov_b64 s[8:9], s[2:3]
	s_branch .Lp1_dd_a
.Lp1_lat_a:
	s_ashr_i32 s10, s24, 31
	s_lshr_b32 s10, s10, 20
	s_add_i32 s10, s24, s10
	s_ashr_i32 s10, s10, 12
	s_add_u32 s20, s42, s12
	s_addc_u32 s21, s43, s13
	s_mul_i32 s8, s10, 0x3000
	s_ashr_i32 s9, s8, 31
	s_lshl_b64 s[8:9], s[8:9], 2
	s_add_u32 s8, s6, s8
	s_addc_u32 s9, s7, s9
	s_add_u32 s18, s8, 0x2000
	s_addc_u32 s19, s9, 0
.Lp1_dd_a:
	global_load_dwordx4 v[200:203], v246, s[20:21] nt
	global_load_dwordx4 v[204:207], v246, s[20:21] offset:1024 nt
	global_load_dwordx4 v[208:211], v246, s[20:21] offset:2048 nt
	global_load_dwordx4 v[212:215], v246, s[20:21] offset:3072 nt
	global_load_dwordx4 v[216:219], v247, s[20:21] nt
	global_load_dwordx4 v[232:235], v247, s[20:21] offset:1024 nt
	global_load_dwordx4 v[236:239], v247, s[20:21] offset:2048 nt
	global_load_dwordx4 v[240:243], v247, s[20:21] offset:3072 nt
	s_waitcnt vmcnt(0)
.Lp1_top:
	s_waitcnt vmcnt(8)
	v_mov_b64_e32 v[126:127], v[200:201]
	v_mov_b64_e32 v[128:129], v[202:203]
	v_mov_b64_e32 v[122:123], v[204:205]
	v_mov_b64_e32 v[124:125], v[206:207]
	v_mov_b64_e32 v[118:119], v[208:209]
	v_mov_b64_e32 v[120:121], v[210:211]
	v_mov_b64_e32 v[114:115], v[212:213]
	v_mov_b64_e32 v[116:117], v[214:215]
	v_mov_b64_e32 v[110:111], v[216:217]
	v_mov_b64_e32 v[112:113], v[218:219]
	v_mov_b64_e32 v[106:107], v[232:233]
	v_mov_b64_e32 v[108:109], v[234:235]
	v_mov_b64_e32 v[102:103], v[236:237]
	v_mov_b64_e32 v[104:105], v[238:239]
	v_mov_b64_e32 v[98:99], v[240:241]
	v_mov_b64_e32 v[100:101], v[242:243]
	s_mov_b32 s38, 0
	s_cmp_eq_u32 s10, s22
	s_cbranch_scc1 .Lp1_same
	global_load_dwordx4 v[42:45], v246, s[18:19]
	global_load_dwordx4 v[50:53], v246, s[18:19] offset:1024
	global_load_dwordx4 v[34:37], v246, s[8:9]
	global_load_dwordx4 v[38:41], v246, s[8:9] offset:1024
	global_load_dwordx4 v[62:65], v246, s[18:19] offset:2048
	global_load_dwordx4 v[66:69], v246, s[18:19] offset:3072
	global_load_dwordx4 v[46:49], v246, s[8:9] offset:2048
	global_load_dwordx4 v[54:57], v246, s[8:9] offset:3072
	global_load_dwordx4 v[78:81], v139, s[18:19]
	global_load_dwordx4 v[58:61], v139, s[8:9]
	global_load_dwordx4 v[86:89], v140, s[18:19]
	global_load_dwordx4 v[70:73], v140, s[8:9]
	global_load_dwordx4 v[90:93], v141, s[18:19]
	global_load_dwordx4 v[74:77], v141, s[8:9]
	global_load_dwordx4 v[94:97], v142, s[18:19]
	global_load_dwordx4 v[82:85], v142, s[8:9]
	s_mov_b32 s22, s10
	s_mov_b32 s38, 1
.Lp1_same:
	s_add_i32 s24, s24, s37
	s_add_u32 s12, s12, s14
	s_addc_u32 s13, s13, s15
	s_cmpk_gt_i32 s24, 0x43ff
	s_cbranch_scc1 .Lp1_nonext
	s_cmpk_gt_i32 s24, 0x3fff
	s_cbranch_scc0 .Lp1_lat_b
	s_add_i32 s10, s24, 0xffffc000
	s_lshl_b64 s[18:19], s[10:11], 13
	s_add_u32 s20, s46, s18
	s_addc_u32 s21, s47, s19
	s_mov_b32 s10, 4
	s_mov_b64 s[18:19], s[4:5]
	s_mov_b64 s[8:9], s[2:3]
	s_branch .Lp1_dd_b

; __device__ __forceinline__ unsigned pk2(float lo, float hi) { typedef float f2v __attribute__((ext_vector_type(2))); typedef __bf16 b2v __attribute__((ext_vector_type(2))); const f2v v = {lo, hi}; return __builtin_bit_cast(unsigned, __builtin_convertvector(v, b2v)); }
; __device__ __forceinline__ float wave_sum(float v) {
; #pragma unroll
;     for (int o = 1; o < 64; o <<= 1) v += __shfl_xor(v, o);
;     return v;
; __global__ void __launch_bounds__(NWAVES * 64, 2) mk_fwd(Args args) {
;     ...
;             for (int j = 0; j < 8; ++j) ss += (v[j].x * v[j].x + v[j].y * v[j].y) + (v[j].z * v[j].z + v[j].w * v[j].w);
;             const float rstd = 1.0f / sqrtf(wave_sum(ss) * (1.f / D) + EPS);
;             v2u* o8 = (v2u*)(HX + (size_t)row * D) + lane;
; #pragma unroll
;             for (int j = 0; j < 8; ++j) { const f32x4 o = (v[j] * rstd * pg[j]) * (ps1[j] + 1.0f) + ps0[j]; v2u w; w.x = pk2(o.x, o.y); w.y = pk2(o.z, o.w); o8[64 * j] = w; }
.Lp1_dd_b:
	global_load_dwordx4 v[200:203], v246, s[20:21] nt
	global_load_dwordx4 v[204:207], v246, s[20:21] offset:1024 nt
	global_load_dwordx4 v[208:211], v246, s[20:21] offset:2048 nt
	global_load_dwordx4 v[212:215], v246, s[20:21] offset:3072 nt
	global_load_dwordx4 v[216:219], v247, s[20:21] nt
	global_load_dwordx4 v[232:235], v247, s[20:21] offset:1024 nt
	global_load_dwordx4 v[236:239], v247, s[20:21] offset:2048 nt
	global_load_dwordx4 v[240:243], v247, s[20:21] offset:3072 nt
	s_branch .Lp1_body
.Lp1_nonext:
	s_waitcnt vmcnt(0)
	s_mov_b32 s38, 0
.Lp1_body:
	v_mov_b32_e32 v148, v127
	v_mov_b32_e32 v149, v123
	v_mov_b32_e32 v146, v126
	v_mov_b32_e32 v147, v122
	v_pk_mul_f32 v[148:149], v[148:149], v[148:149]
	v_mov_b32_e32 v150, v129
	v_mov_b32_e32 v151, v125
	v_pk_fma_f32 v[146:147], v[146:147], v[146:147], v[148:149]
	v_mov_b32_e32 v148, v128
	v_mov_b32_e32 v149, v124
	v_pk_mul_f32 v[150:151], v[150:151], v[150:151]
	v_mul_f32_e32 v130, v110, v110
	v_pk_fma_f32 v[148:149], v[148:149], v[148:149], v[150:151]
	v_pk_mul_f32 v[150:151], v[118:119], v[118:119]
	v_pk_add_f32 v[146:147], v[146:147], v[148:149]
	v_pk_mul_f32 v[148:149], v[120:121], v[120:121]
	v_mul_f32_e32 v145, v111, v111
	v_pk_mov_b32 v[152:153], v[150:151], v[148:149] op_sel:[1,0]
	v_mov_b32_e32 v151, v149
	v_pk_add_f32 v[148:149], v[152:153], v[150:151]
	v_pk_add_f32 v[146:147], v[146:147], v[146:147] op_sel:[0,1] op_sel_hi:[1,0]
	v_pk_add_f32 v[148:149], v[148:149], v[148:149] op_sel:[0,1] op_sel_hi:[1,0]
	v_mov_b32_e32 v147, v130
	v_mov_b32_e32 v149, v145
	v_mul_f32_e32 v130, v115, v115
	v_mul_f32_e32 v150, v112, v112
	v_pk_add_f32 v[146:147], v[146:147], v[148:149]
	v_pk_fma_f32 v[148:149], v[114:115], v[114:115], v[130:131] op_sel_hi:[1,1,0]
	v_mul_f32_e32 v130, v117, v117
	v_mul_f32_e32 v152, v113, v113
	v_mov_b32_e32 v149, v150
	v_pk_fma_f32 v[150:151], v[116:117], v[116:117], v[130:131] op_sel_hi:[1,1,0]
	v_mul_f32_e32 v130, v98, v98
	v_mov_b32_e32 v151, v152
	v_pk_add_f32 v[148:149], v[148:149], v[150:151]
	v_pk_mul_f32 v[150:151], v[106:107], v[106:107]
	v_pk_add_f32 v[146:147], v[146:147], v[148:149]
	v_pk_mul_f32 v[148:149], v[108:109], v[108:109]
	v_mul_f32_e32 v145, v99, v99
	v_pk_mov_b32 v[152:153], v[150:151], v[148:149] op_sel:[1,0]
	v_mov_b32_e32 v151, v149
	v_pk_add_f32 v[148:149], v[152:153], v[150:151]
	v_pk_add_f32 v[146:147], v[146:147], v[146:147] op_sel:[0,1] op_sel_hi:[1,0]
	v_pk_add_f32 v[148:149], v[148:149], v[148:149] op_sel:[0,1] op_sel_hi:[1,0]
	v_mov_b32_e32 v147, v130
	v_mov_b32_e32 v149, v145
	v_mul_f32_e32 v130, v103, v103
	v_mul_f32_e32 v150, v100, v100
	v_pk_add_f32 v[146:147], v[146:147], v[148:149]
	v_pk_fma_f32 v[148:149], v[102:103], v[102:103], v[130:131] op_sel_hi:[1,1,0]
	v_mul_f32_e32 v130, v105, v105
	v_mul_f32_e32 v152, v101, v101
	v_mov_b32_e32 v149, v150
	v_pk_fma_f32 v[150:151], v[104:105], v[104:105], v[130:131] op_sel_hi:[1,1,0]
	s_nop 0
	v_mov_b32_e32 v151, v152
	v_pk_add_f32 v[148:149], v[148:149], v[150:151]
	s_nop 0
	v_pk_add_f32 v[146:147], v[146:147], v[148:149]
	s_nop 0
	v_add_f32_e32 v130, v146, v147
	ds_bpermute_b32 v145, v1, v130
	s_waitcnt lgkmcnt(0)
	v_add_f32_e32 v130, v130, v145
	ds_bpermute_b32 v145, v134, v130
	s_waitcnt lgkmcnt(0)
	v_add_f32_e32 v130, v130, v145
	ds_bpermute_b32 v145, v135, v130
	s_waitcnt lgkmcnt(0)
	v_add_f32_e32 v130, v130, v145
	ds_bpermute_b32 v145, v136, v130
	s_waitcnt lgkmcnt(0)
	v_add_f32_e32 v130, v130, v145
	ds_bpermute_b32 v145, v137, v130
	s_waitcnt lgkmcnt(0)
	v_add_f32_e32 v130, v130, v145
	ds_bpermute_b32 v145, v138, v130
	s_waitcnt lgkmcnt(0)
	v_add_f32_e32 v130, v130, v145
	v_fmamk_f32 v130, v130, 0x3a000000, v143
	v_mul_f32_e32 v145, 0x4f800000, v130
	v_cmp_gt_f32_e32 vcc, s23, v130
	s_nop 1
	v_cndmask_b32_e32 v130, v130, v145, vcc
	v_sqrt_f32_e32 v145, v130
	s_nop 0
	v_add_u32_e32 v146, -1, v145
	v_fma_f32 v147, -v146, v145, v130
	v_cmp_ge_f32_e64 s[40:41], 0, v147
	v_add_u32_e32 v147, 1, v145
	s_nop 0
	v_cndmask_b32_e64 v146, v145, v146, s[40:41]
	v_fma_f32 v145, -v147, v145, v130
	v_cmp_lt_f32_e64 s[40:41], 0, v145
	s_nop 1
	v_cndmask_b32_e64 v145, v146, v147, s[40:41]
	v_mul_f32_e32 v146, 0x37800000, v145
	v_cndmask_b32_e32 v145, v145, v146, vcc
	v_cmp_class_f32_e32 vcc, v130, v144
	s_nop 1
	v_cndmask_b32_e32 v130, v145, v130, vcc
	v_div_scale_f32 v145, s[40:41], v130, v130, 1.0
	v_rcp_f32_e32 v146, v145
	s_nop 1
	v_fma_f32 v147, -v145, v146, 1.0
	v_fmac_f32_e32 v146, v147, v146
	v_div_scale_f32 v147, vcc, 1.0, v130, 1.0
	v_mul_f32_e32 v148, v147, v146
	v_fma_f32 v149, -v145, v148, v147
	v_fmac_f32_e32 v148, v149, v146
	v_fma_f32 v145, -v145, v148, v147
	v_div_fmas_f32 v145, v145, v146, v148
	v_div_fixup_f32 v130, v145, v130, 1.0
	v_pk_mul_f32 v[128:129], v[130:131], v[128:129] op_sel_hi:[0,1]
	v_pk_mul_f32 v[126:127], v[130:131], v[126:127] op_sel_hi:[0,1]
	v_pk_mul_f32 v[126:127], v[126:127], v[2:3]
	v_pk_mul_f32 v[128:129], v[128:129], v[4:5]
	s_cmp_eq_u32 s38, 0
	s_cbranch_scc1 .Lp1_nowait
	s_waitcnt vmcnt(8)
; __device__ __forceinline__ unsigned pk2(float lo, float hi) { typedef float f2v __attribute__((ext_vector_type(2))); typedef __bf16 b2v __attribute__((ext_vector_type(2))); const f2v v = {lo, hi}; return __builtin_bit_cast(unsigned, __builtin_convertvector(v, b2v)); }
; #define in_x KARG(0)
; #define ctx KARG(2)
; __global__ void __launch_bounds__(NWAVES * 64, 2) mk_fwd(Args args) {
;     ...
;         for (int row = gw; row < MT; row += NGW) {
;             const float* src; const float* sh; const float* sc; int b;
;             if (row < M) { b = row / SEQ; src = in_x + (size_t)row * D; sh = MODX + b * MODW; sc = sh + D; }
;             else { b = NB; src = ctx + (size_t)(row - M) * D; sh = MODC; sc = MODC + D; }
;             f32x4 v[8]; float ss = 0.f;
; #pragma unroll
;             for (int j = 0; j < 8; ++j) v[j] = __builtin_nontemporal_load((const f32x4*)src + lane + 64 * j);
;             if (b != bcur) { bcur = b;
; #pragma unroll
;                 for (int j = 0; j < 8; ++j) { ps1[j] = ((const f32x4*)sc)[lane + 64 * j]; ps0[j] = ((const f32x4*)sh)[lane + 64 * j]; } }
; #pragma unroll
;             for (int j = 0; j < 8; ++j) ss += (v[j].x * v[j].x + v[j].y * v[j].y) + (v[j].z * v[j].z + v[j].w * v[j].w);
;             const float rstd = 1.0f / sqrtf(wave_sum(ss) * (1.f / D) + EPS);
;             v2u* o8 = (v2u*)(HX + (size_t)row * D) + lane;
; #pragma unroll
;             for (int j = 0; j < 8; ++j) { const f32x4 o = (v[j] * rstd * pg[j]) * (ps1[j] + 1.0f) + ps0[j]; v2u w; w.x = pk2(o.x, o.y); w.y = pk2(o.z, o.w); o8[64 * j] = w; }
.Lp1_nowait:
	v_pk_add_f32 v[146:147], v[44:45], 1.0 op_sel_hi:[1,0]
	v_pk_add_f32 v[148:149], v[42:43], 1.0 op_sel_hi:[1,0]
	v_pk_fma_f32 v[128:129], v[128:129], v[146:147], v[36:37]
	v_pk_fma_f32 v[126:127], v[126:127], v[148:149], v[34:35]
	v_pk_mul_f32 v[124:125], v[130:131], v[124:125] op_sel_hi:[0,1]
	v_cvt_pk_bf16_f32 v126, v126, v127
	v_cvt_pk_bf16_f32 v127, v128, v129
	v_pk_mul_f32 v[122:123], v[130:131], v[122:123] op_sel_hi:[0,1]
	global_store_dwordx2 v[132:133], v[126:127], off offset:-3584
	v_pk_mul_f32 v[122:123], v[122:123], v[6:7]
	v_pk_mul_f32 v[124:125], v[124:125], v[8:9]
	v_pk_add_f32 v[126:127], v[52:53], 1.0 op_sel_hi:[1,0]
	v_pk_add_f32 v[128:129], v[50:51], 1.0 op_sel_hi:[1,0]
	v_pk_fma_f32 v[124:125], v[124:125], v[126:127], v[40:41]
	v_pk_fma_f32 v[122:123], v[122:123], v[128:129], v[38:39]
	v_pk_mul_f32 v[120:121], v[130:131], v[120:121] op_sel_hi:[0,1]
	v_cvt_pk_bf16_f32 v122, v122, v123
	v_cvt_pk_bf16_f32 v123, v124, v125
	v_pk_mul_f32 v[118:119], v[130:131], v[118:119] op_sel_hi:[0,1]
	global_store_dwordx2 v[132:133], v[122:123], off offset:-3072
	v_pk_mul_f32 v[118:119], v[118:119], v[10:11]
	v_pk_mul_f32 v[120:121], v[120:121], v[12:13]
	v_pk_add_f32 v[122:123], v[64:65], 1.0 op_sel_hi:[1,0]
	v_pk_add_f32 v[124:125], v[62:63], 1.0 op_sel_hi:[1,0]
	v_pk_fma_f32 v[120:121], v[120:121], v[122:123], v[48:49]
	v_pk_fma_f32 v[118:119], v[118:119], v[124:125], v[46:47]
	v_pk_mul_f32 v[116:117], v[130:131], v[116:117] op_sel_hi:[0,1]
	v_cvt_pk_bf16_f32 v118, v118, v119
	v_cvt_pk_bf16_f32 v119, v120, v121
	v_pk_mul_f32 v[114:115], v[130:131], v[114:115] op_sel_hi:[0,1]
	global_store_dwordx2 v[132:133], v[118:119], off offset:-2560
	v_pk_mul_f32 v[114:115], v[114:115], v[14:15]
	v_pk_mul_f32 v[116:117], v[116:117], v[16:17]
	v_pk_add_f32 v[118:119], v[68:69], 1.0 op_sel_hi:[1,0]
	v_pk_add_f32 v[120:121], v[66:67], 1.0 op_sel_hi:[1,0]
	v_pk_fma_f32 v[116:117], v[116:117], v[118:119], v[56:57]
	v_pk_fma_f32 v[114:115], v[114:115], v[120:121], v[54:55]
	v_pk_mul_f32 v[112:113], v[130:131], v[112:113] op_sel_hi:[0,1]
	v_cvt_pk_bf16_f32 v114, v114, v115
	v_cvt_pk_bf16_f32 v115, v116, v117
	v_pk_mul_f32 v[110:111], v[130:131], v[110:111] op_sel_hi:[0,1]
	global_store_dwordx2 v[132:133], v[114:115], off offset:-2048
	v_pk_mul_f32 v[110:111], v[110:111], v[18:19]
	v_pk_mul_f32 v[112:113], v[112:113], v[20:21]
	v_pk_add_f32 v[114:115], v[80:81], 1.0 op_sel_hi:[1,0]
	v_pk_add_f32 v[116:117], v[78:79], 1.0 op_sel_hi:[1,0]
	v_pk_fma_f32 v[112:113], v[112:113], v[114:115], v[60:61]
	v_pk_fma_f32 v[110:111], v[110:111], v[116:117], v[58:59]
	v_pk_mul_f32 v[108:109], v[130:131], v[108:109] op_sel_hi:[0,1]
	v_cvt_pk_bf16_f32 v110, v110, v111
	v_cvt_pk_bf16_f32 v111, v112, v113
	v_pk_mul_f32 v[106:107], v[130:131], v[106:107] op_sel_hi:[0,1]
	global_store_dwordx2 v[132:133], v[110:111], off offset:-1536
	v_pk_mul_f32 v[106:107], v[106:107], v[22:23]
	v_pk_mul_f32 v[108:109], v[108:109], v[24:25]
	v_pk_add_f32 v[110:111], v[88:89], 1.0 op_sel_hi:[1,0]
	v_pk_add_f32 v[112:113], v[86:87], 1.0 op_sel_hi:[1,0]
	v_pk_fma_f32 v[108:109], v[108:109], v[110:111], v[72:73]
	v_pk_fma_f32 v[106:107], v[106:107], v[112:113], v[70:71]
	v_pk_mul_f32 v[104:105], v[130:131], v[104:105] op_sel_hi:[0,1]
	v_cvt_pk_bf16_f32 v106, v106, v107
	v_cvt_pk_bf16_f32 v107, v108, v109
	v_pk_mul_f32 v[102:103], v[130:131], v[102:103] op_sel_hi:[0,1]
	global_store_dwordx2 v[132:133], v[106:107], off offset:-1024
	v_pk_mul_f32 v[102:103], v[102:103], v[26:27]
	v_pk_mul_f32 v[104:105], v[104:105], v[28:29]
	v_pk_add_f32 v[106:107], v[92:93], 1.0 op_sel_hi:[1,0]
	v_pk_add_f32 v[108:109], v[90:91], 1.0 op_sel_hi:[1,0]
	v_pk_fma_f32 v[104:105], v[104:105], v[106:107], v[76:77]
	v_pk_fma_f32 v[102:103], v[102:103], v[108:109], v[74:75]
	v_pk_mul_f32 v[100:101], v[130:131], v[100:101] op_sel_hi:[0,1]
	v_cvt_pk_bf16_f32 v102, v102, v103
	v_cvt_pk_bf16_f32 v103, v104, v105
	v_pk_mul_f32 v[98:99], v[130:131], v[98:99] op_sel_hi:[0,1]
	global_store_dwordx2 v[132:133], v[102:103], off offset:-512
	v_pk_mul_f32 v[98:99], v[98:99], v[30:31]
	v_pk_mul_f32 v[100:101], v[100:101], v[32:33]
	v_pk_add_f32 v[102:103], v[96:97], 1.0 op_sel_hi:[1,0]
	v_pk_add_f32 v[104:105], v[94:95], 1.0 op_sel_hi:[1,0]
	v_pk_fma_f32 v[100:101], v[100:101], v[102:103], v[84:85]
	v_pk_fma_f32 v[98:99], v[98:99], v[104:105], v[82:83]
	v_cvt_pk_bf16_f32 v98, v98, v99
	v_cvt_pk_bf16_f32 v99, v100, v101
	global_store_dwordx2 v[132:133], v[98:99], off
	v_lshl_add_u64 v[132:133], v[132:133], 0, s[16:17]
	s_cmpk_gt_i32 s24, 0x43ff
	s_cbranch_scc0 .Lp1_top
